# baseline (speedup 1.0000x reference)
_Z15k_scatter_gemm1PKiS0_PiPjPyPKfPK6__halfS5_S5_PS6_PfSA_:
	s_cmpk_gt_u32 s2, 0x186
	s_mov_b64 s[4:5], -1
	s_cbranch_scc0 .LBB1_22
	s_load_dwordx2 s[26:27], s[0:1], 0x28
	s_load_dwordx2 s[10:11], s[0:1], 0x30
	s_load_dwordx4 s[28:31], s[0:1], 0x38
	v_lshlrev_b32_e32 v92, 4, v0
	v_add_u32_e32 v93, 0x1000, v92
	v_add_u32_e32 v94, 0x2000, v92
	v_add_u32_e32 v95, 0x3000, v92
	v_add_u32_e32 v96, 0x4000, v92
	v_add_u32_e32 v97, 0x5000, v92
	v_add_u32_e32 v98, 0x6000, v92
	v_add_u32_e32 v99, 0x7000, v92
	v_add_u32_e32 v100, 0x8000, v92
	v_lshlrev_b32_e32 v101, 2, v0
	s_movk_i32 s3, 0x80
	v_cmp_gt_u32_e64 s[8:9], s3, v0
	s_waitcnt lgkmcnt(0)
	global_load_dwordx4 v[104:107], v92, s[10:11]
	global_load_dwordx4 v[108:111], v93, s[10:11]
	global_load_dwordx4 v[112:115], v94, s[10:11]
	global_load_dwordx4 v[116:119], v95, s[10:11]
	global_load_dwordx4 v[120:123], v96, s[10:11]
	global_load_dwordx4 v[124:127], v97, s[10:11]
	global_load_dwordx4 v[128:131], v98, s[10:11]
	global_load_dwordx4 v[132:135], v99, s[10:11]
	s_and_saveexec_b64 s[4:5], s[8:9]
	global_load_dwordx4 v[136:139], v100, s[10:11]
	global_load_dword v140, v101, s[28:29]
	global_load_dword v141, v101, s[30:31]
	s_mov_b64 exec, s[4:5]
	s_lshl_b32 s3, s2, 2
	v_lshrrev_b32_e32 v14, 6, v0
	s_add_i32 s4, s3, 0xfffff9e4
	v_or_b32_e32 v2, s4, v14
	s_movk_i32 s4, 2500
	v_cmp_gt_i32_e32 vcc, s4, v2
	v_and_b32_e32 v1, 15, v0
	v_and_b32_e32 v66, 48, v0
	v_mov_b32_e32 v67, 0
	s_and_saveexec_b64 s[6:7], vcc
	s_cbranch_execz .Lg1_noval
	v_lshl_or_b32 v2, v2, 4, v1
	v_ashrrev_i32_e32 v3, 31, v2
	v_lshlrev_b64 v[2:3], 9, v[2:3]
	v_lshl_add_u64 v[2:3], s[26:27], 0, v[2:3]
	v_lshl_add_u64 v[16:17], v[2:3], 0, v[66:67]
	global_load_dwordx4 v[38:41], v[16:17], off offset:448
	global_load_dwordx4 v[34:37], v[16:17], off offset:384
	global_load_dwordx4 v[46:49], v[16:17], off offset:320
	global_load_dwordx4 v[42:45], v[16:17], off offset:256
	global_load_dwordx4 v[6:9], v[16:17], off offset:192
	global_load_dwordx4 v[18:21], v[16:17], off offset:128
	global_load_dwordx4 v[2:5], v[16:17], off offset:64
	global_load_dwordx4 v[10:13], v[16:17], off
	s_mov_b64 exec, s[6:7]
	s_waitcnt vmcnt(8)
	s_branch .Lg1_stage
.Lg1_noval:
	s_mov_b64 exec, s[6:7]
	s_waitcnt vmcnt(0)
.Lg1_stage:
	ds_write_b128 v92, v[104:107]
	ds_write_b128 v92, v[108:111] offset:4096
	ds_write_b128 v92, v[112:115] offset:8192
	ds_write_b128 v92, v[116:119] offset:12288
	ds_write_b128 v92, v[120:123] offset:16384
	ds_write_b128 v92, v[124:127] offset:20480
	ds_write_b128 v92, v[128:131] offset:24576
	ds_write_b128 v92, v[132:135] offset:28672
	s_and_saveexec_b64 s[4:5], s[8:9]
	ds_write_b128 v92, v[136:139] offset:32768
	ds_write2st64_b32 v101, v140, v141 offset0:204 offset1:206
	s_mov_b64 exec, s[4:5]
	s_waitcnt lgkmcnt(0)
	s_barrier
	s_and_saveexec_b64 s[6:7], vcc
	s_cbranch_execz .LBB1_21
	s_load_dwordx2 s[8:9], s[0:1], 0x58
	s_load_dwordx2 s[10:11], s[0:1], 0x48
	v_and_b32_e32 v15, 63, v0
	v_lshl_add_u64 v[68:69], s[26:27], 0, v[66:67]
	s_movk_i32 s4, 0x1100
	v_cmp_gt_u32_e32 vcc, 16, v15
	v_mul_u32_u24_e32 v15, 0x110, v1
	v_mul_u32_u24_e32 v17, 0x1100, v14
	v_mad_u32_u24 v22, v14, s4, v15
	v_lshlrev_b32_e32 v16, 4, v1
	v_add_u32_e32 v25, s3, v14
	v_lshlrev_b32_e32 v14, 4, v14
	v_bfe_u32 v80, v0, 4, 2
	v_or_b32_e32 v24, v17, v16
	v_mov_b32_e32 v17, v67
	v_lshl_or_b32 v82, s2, 6, v14
	v_mbcnt_lo_u32_b32 v14, -1, 0
	s_waitcnt lgkmcnt(0)
	v_lshl_add_u64 v[70:71], s[10:11], 0, v[16:17]
	v_or_b32_e32 v17, 4, v80
	v_mbcnt_hi_u32_b32 v84, -1, v14
	v_lshlrev_b32_e32 v23, 3, v80
	v_mul_u32_u24_e32 v16, 0x110, v80
	v_mul_u32_u24_e32 v17, 0x110, v17
	v_and_b32_e32 v14, 64, v84
	v_subrev_u32_e32 v67, 56, v25
	v_or_b32_e32 v81, 0xffff9e40, v1
	s_mov_b64 s[10:11], 0
	s_movk_i32 s3, 992
	v_add_u32_e32 v83, v66, v15
	v_xor_b32_e32 v85, 16, v84
	v_add_u32_e32 v86, 64, v14
	v_xor_b32_e32 v87, 32, v84
	v_add_u32_e32 v88, v22, v23
	v_add_u32_e32 v89, v24, v16
	v_add_u32_e32 v90, v24, v17
	s_movk_i32 s12, 991
	s_waitcnt vmcnt(0)
	s_branch .LBB1_19

.LBB1_28:
	s_mov_b32 s23, s22
	s_or_b64 s[4:5], s[22:23], s[8:9]
	v_cmp_le_u32_e64 s[0:1], s5, v1
	v_cmp_le_u32_e64 s[4:5], s4, v2
	s_and_saveexec_b64 s[24:25], s[4:5]
	ds_write_b32 v3, v4
	s_or_b64 exec, exec, s[24:25]
	s_and_saveexec_b64 s[4:5], s[0:1]
	s_cbranch_execz .LBB1_27
	ds_write_b32 v3, v4 offset:1024
	s_branch .LBB1_27
.LBB1_35:
	s_or_b64 exec, exec, s[10:11]
	v_mov_b32_e32 v34, v40

_Z12k_fine_gemm1PKjPKyPKiPiS5_S5_S5_PKfPK6__halfS7_S7_PS8_PfSC_:
	s_cmpk_gt_u32 s2, 0x186
	s_mov_b64 s[4:5], -1
	s_cbranch_scc0 .LBB2_22
	s_load_dwordx2 s[26:27], s[0:1], 0x38
	s_load_dwordx2 s[10:11], s[0:1], 0x40
	s_load_dwordx4 s[28:31], s[0:1], 0x48
	v_lshlrev_b32_e32 v92, 4, v0
	v_add_u32_e32 v93, 0x1000, v92
	v_add_u32_e32 v94, 0x2000, v92
	v_add_u32_e32 v95, 0x3000, v92
	v_add_u32_e32 v96, 0x4000, v92
	v_add_u32_e32 v97, 0x5000, v92
	v_add_u32_e32 v98, 0x6000, v92
	v_add_u32_e32 v99, 0x7000, v92
	v_add_u32_e32 v100, 0x8000, v92
	v_lshlrev_b32_e32 v101, 2, v0
	s_movk_i32 s3, 0x80
	v_cmp_gt_u32_e64 s[8:9], s3, v0
	s_waitcnt lgkmcnt(0)
	global_load_dwordx4 v[104:107], v92, s[10:11]
	global_load_dwordx4 v[108:111], v93, s[10:11]
	global_load_dwordx4 v[112:115], v94, s[10:11]
	global_load_dwordx4 v[116:119], v95, s[10:11]
	global_load_dwordx4 v[120:123], v96, s[10:11]
	global_load_dwordx4 v[124:127], v97, s[10:11]
	global_load_dwordx4 v[128:131], v98, s[10:11]
	global_load_dwordx4 v[132:135], v99, s[10:11]
	s_and_saveexec_b64 s[4:5], s[8:9]
	global_load_dwordx4 v[136:139], v100, s[10:11]
	global_load_dword v140, v101, s[28:29]
	global_load_dword v141, v101, s[30:31]
	s_mov_b64 exec, s[4:5]
	s_lshl_b32 s3, s2, 2
	v_lshrrev_b32_e32 v14, 6, v0
	s_addk_i32 s3, 936
	v_add_u32_e32 v1, s3, v14
	s_movk_i32 s3, 0x186a
	v_cmp_gt_i32_e32 vcc, s3, v1
	v_and_b32_e32 v80, 15, v0
	v_and_b32_e32 v66, 48, v0
	v_mov_b32_e32 v67, 0
	s_and_saveexec_b64 s[6:7], vcc
	s_cbranch_execz .Lg2_noval
	v_lshl_or_b32 v2, v1, 4, v80
	v_ashrrev_i32_e32 v3, 31, v2
	v_lshlrev_b64 v[2:3], 9, v[2:3]
	v_lshl_add_u64 v[2:3], s[26:27], 0, v[2:3]
	v_lshl_add_u64 v[16:17], v[2:3], 0, v[66:67]
	global_load_dwordx4 v[38:41], v[16:17], off offset:448
	global_load_dwordx4 v[34:37], v[16:17], off offset:384
	global_load_dwordx4 v[26:29], v[16:17], off offset:320
	global_load_dwordx4 v[30:33], v[16:17], off offset:256
	global_load_dwordx4 v[6:9], v[16:17], off offset:192
	global_load_dwordx4 v[18:21], v[16:17], off offset:128
	global_load_dwordx4 v[2:5], v[16:17], off offset:64
	global_load_dwordx4 v[10:13], v[16:17], off
	s_mov_b64 exec, s[6:7]
	s_waitcnt vmcnt(8)
	s_branch .Lg2_stage

.Lg2_stage:
	ds_write_b128 v92, v[104:107]
	ds_write_b128 v92, v[108:111] offset:4096
	ds_write_b128 v92, v[112:115] offset:8192
	ds_write_b128 v92, v[116:119] offset:12288
	ds_write_b128 v92, v[120:123] offset:16384
	ds_write_b128 v92, v[124:127] offset:20480
	ds_write_b128 v92, v[128:131] offset:24576
	ds_write_b128 v92, v[132:135] offset:28672
	s_and_saveexec_b64 s[4:5], s[8:9]
	ds_write_b128 v92, v[136:139] offset:32768
	ds_write2st64_b32 v101, v140, v141 offset0:204 offset1:206
	s_mov_b64 exec, s[4:5]
	s_waitcnt lgkmcnt(0)
	s_barrier
	s_and_saveexec_b64 s[6:7], vcc
	s_cbranch_execz .LBB2_21
	s_load_dwordx2 s[8:9], s[0:1], 0x68
	s_load_dwordx2 s[10:11], s[0:1], 0x58
	v_and_b32_e32 v15, 63, v0
	s_movk_i32 s3, 0x1100
	v_cmp_gt_u32_e32 vcc, 16, v15
	v_mul_u32_u24_e32 v15, 0x110, v80
	v_mul_u32_u24_e32 v17, 0x1100, v14
	v_mad_u32_u24 v22, v14, s3, v15
	v_lshlrev_b32_e32 v16, 4, v80
	v_lshlrev_b32_e32 v14, 4, v14
	v_bfe_u32 v81, v0, 4, 2
	v_or_b32_e32 v24, v17, v16
	v_mov_b32_e32 v17, v67
	v_lshl_or_b32 v82, s2, 6, v14
	v_mbcnt_lo_u32_b32 v14, -1, 0
	s_waitcnt lgkmcnt(0)
	v_lshl_add_u64 v[70:71], s[10:11], 0, v[16:17]
	v_or_b32_e32 v17, 4, v81
	v_mbcnt_hi_u32_b32 v84, -1, v14
	v_lshlrev_b32_e32 v23, 3, v81
	v_mul_u32_u24_e32 v16, 0x110, v81
	v_mul_u32_u24_e32 v17, 0x110, v17
	v_and_b32_e32 v14, 64, v84
	v_lshl_add_u64 v[68:69], s[26:27], 0, v[66:67]
	v_or_b32_e32 v67, 0x3a80, v80
	s_mov_b64 s[10:11], 0
	s_movk_i32 s3, 0x1285
	s_movk_i32 s14, 0x1286
	v_add_u32_e32 v83, v66, v15
	v_xor_b32_e32 v85, 16, v84
	v_add_u32_e32 v86, 64, v14
	v_xor_b32_e32 v87, 32, v84
	v_add_u32_e32 v88, v22, v23
	v_add_u32_e32 v89, v24, v16
	v_add_u32_e32 v90, v24, v17
	s_waitcnt vmcnt(0)
	s_branch .LBB2_19

.LBB2_168:
	s_or_b64 exec, exec, s[0:1]
	s_and_saveexec_b64 s[0:1], s[66:67]
	s_cbranch_execnz .LBB2_219
	s_branch .LBB2_223
.LBB2_172:
	v_lshlrev_b32_e32 v4, 2, v9
	global_load_dword v39, v4, s[66:67]
	s_or_b64 exec, exec, s[70:71]
	s_and_saveexec_b64 s[66:67], s[48:49]
	s_cbranch_execz .LBB2_95

_Z6k_agg2PKiS0_PK6__halfPKfS5_S5_PfS5_S0_S0_:
	s_and_b32 s3, s2, 7
	s_mul_i32 s8, s3, 0x30d
	s_min_u32 s3, s3, 2
	s_lshr_b32 s2, s2, 3
	s_add_i32 s2, s3, s2
	s_load_dwordx4 s[4:7], s[0:1], 0x38
	v_lshrrev_b32_e32 v1, 6, v0
	s_add_i32 s2, s2, s8
	s_lshl_b32 s12, s2, 4
	v_lshlrev_b32_e32 v2, 2, v1
	v_bfe_u32 v3, v0, 4, 2
	v_or3_b32 v2, s12, v2, v3
	v_ashrrev_i32_e32 v3, 31, v2
	v_lshlrev_b64 v[10:11], 2, v[2:3]
	s_load_dwordx2 s[2:3], s[0:1], 0x48
	s_waitcnt lgkmcnt(0)
	v_lshl_add_u64 v[2:3], s[6:7], 0, v[10:11]
	global_load_dword v17, v[2:3], off
	s_load_dwordx4 s[8:11], s[0:1], 0x20
	s_load_dwordx2 s[16:17], s[0:1], 0x8
	v_and_b32_e32 v29, 3, v0
	v_mov_b32_e32 v15, 0
	v_bfe_u32 v16, v0, 2, 2
	v_lshlrev_b32_e32 v14, 5, v29
	global_load_dwordx4 v[2:5], v14, s[4:5] offset:16
	global_load_dwordx4 v[6:9], v14, s[4:5]
	s_waitcnt lgkmcnt(0)
	v_lshl_add_u64 v[12:13], s[10:11], 0, v[14:15]
	v_lshlrev_b32_e32 v14, 3, v16
	v_lshl_add_u64 v[22:23], v[12:13], 0, v[14:15]
	v_lshl_add_u64 v[10:11], s[2:3], 0, v[10:11]
	global_load_dword v19, v[10:11], off
	v_mov_b32_e32 v41, 0
	s_waitcnt vmcnt(3)
	v_add_u32_sdwa v12, sext(v17), s12 dst_sel:DWORD dst_unused:UNUSED_PAD src0_sel:BYTE_3 src1_sel:DWORD
	v_ashrrev_i32_e32 v13, 31, v12
	v_lshl_add_u64 v[24:25], v[12:13], 2, s[8:9]
	global_load_dword v21, v[24:25], off
	global_load_dwordx2 v[10:11], v[22:23], off
	v_and_b32_e32 v23, 15, v0
	v_and_b32_e32 v24, 0xffffff, v17
	v_add_u32_e32 v14, v24, v23
	s_waitcnt vmcnt(2)
	v_cmp_lt_i32_e32 vcc, v14, v19
	s_and_saveexec_b64 s[2:3], vcc
	s_cbranch_execz .LBB4_2
	v_lshlrev_b32_e32 v14, 2, v14
	global_load_dword v41, v14, s[16:17] nt

.LBB4_5:
	v_add_u32_e32 v4, v23, v24
	v_add_u32_e32 v0, 16, v4
	s_waitcnt vmcnt(0)
	ds_write_b32 v30, v41
	v_cmp_lt_i32_e64 s[2:3], v0, v19
	v_mov_b32_e32 v41, 0
	s_and_saveexec_b64 s[4:5], s[2:3]
	s_cbranch_execz .LBB4_4
	v_lshl_add_u64 v[0:1], v[4:5], 2, s[16:17]
	global_load_dword v41, v[0:1], off offset:64 nt
	s_branch .LBB4_4

.LBB4_18:
	s_or_b64 exec, exec, s[2:3]
	v_add_f32_e32 v2, v2, v7
	v_rcp_f32_e32 v5, v2
	v_lshlrev_b64 v[2:3], 7, v[12:13]
	v_lshlrev_b32_e32 v4, 2, v17
	s_waitcnt lgkmcnt(0)
	v_lshl_add_u64 v[2:3], s[4:5], 0, v[2:3]
	v_cndmask_b32_e32 v6, 0, v5, vcc
	v_mov_b32_e32 v5, 0
	v_lshl_add_u64 v[2:3], v[2:3], 0, v[4:5]
	v_lshlrev_b32_e32 v4, 2, v14
	v_lshl_add_u64 v[2:3], v[2:3], 0, v[4:5]
	s_waitcnt vmcnt(0)
	v_pk_fma_f32 v[0:1], v[0:1], v[6:7], v[10:11] op_sel_hi:[1,0,1]
	global_store_dwordx2 v[2:3], v[0:1], off nt
	s_endpgm
